# speedup vs baseline: 1.0020x; 1.0020x over previous
.LBB3_6:
	v_pk_add_f16 v9, v9, v16
	v_pk_add_f16 v8, v8, v15
	v_pk_fma_f16 v4, v4, v15, v12
	v_rcp_f16_e32 v12, v9
	v_rcp_f16_sdwa v9, v9 dst_sel:DWORD dst_unused:UNUSED_PAD src0_sel:WORD_1
	v_pk_add_f16 v6, v6, v14
	v_pk_fma_f16 v5, v5, v16, v13
	v_rcp_f16_e32 v13, v8
	v_rcp_f16_sdwa v8, v8 dst_sel:DWORD dst_unused:UNUSED_PAD src0_sel:WORD_1
	v_pk_add_f16 v7, v7, v17
	v_pk_fma_f16 v2, v2, v14, v10
	v_rcp_f16_e32 v10, v6
	v_rcp_f16_sdwa v6, v6 dst_sel:DWORD dst_unused:UNUSED_PAD src0_sel:WORD_1
	v_pk_fma_f16 v3, v3, v17, v11
	v_rcp_f16_e32 v11, v7
	v_rcp_f16_sdwa v7, v7 dst_sel:DWORD dst_unused:UNUSED_PAD src0_sel:WORD_1
	v_pack_b32_f16 v9, v12, v9
	v_pk_mul_f16 v9, v5, v9
	v_pack_b32_f16 v5, v13, v8
	v_pk_mul_f16 v8, v4, v5
	v_pack_b32_f16 v4, v10, v6
	v_pk_mul_f16 v6, v2, v4
	v_pack_b32_f16 v2, v11, v7
	v_pk_mul_f16 v7, v3, v2
	v_pk_max_f16 v2, v113, v113
	v_add_u32_e32 v10, v168, v160
	v_pk_max_f16 v5, v2, 0
	v_pk_max_f16 v2, v112, v112
	s_add_i32 s10, s10, -1
	v_pk_max_f16 v4, v2, 0
	v_pk_max_f16 v2, v111, v111
	s_add_i32 s33, s33, 8
	v_pk_max_f16 v3, v2, 0
	v_pk_max_f16 v2, v110, v110
	v_add_u32_e32 v168, 0x8000, v168
	v_pk_max_f16 v2, v2, 0
	ds_write_b128 v10, v[2:5]
	v_pk_max_f16 v2, v65, v65
	v_bitop3_b32 v10, v166, v159, 15 bitop3:0x6c
	v_pk_max_f16 v5, v2, 0
	v_pk_max_f16 v2, v64, v64
	v_lshlrev_b32_e32 v10, 4, v10
	v_pk_max_f16 v4, v2, 0
	v_pk_max_f16 v2, v63, v63
	v_add3_u32 v10, v160, v10, v167
	v_pk_max_f16 v3, v2, 0
	v_pk_max_f16 v2, v62, v62
	v_add_u32_e32 v166, 64, v166
	v_pk_max_f16 v2, v2, 0
	ds_write_b128 v10, v[2:5]
	v_pk_max_f16 v2, v25, v25
	v_add_u32_e32 v10, v170, v160
	v_pk_max_f16 v5, v2, 0
	v_pk_max_f16 v2, v24, v24
	v_add_u32_e32 v170, 0x8000, v170
	v_pk_max_f16 v4, v2, 0
	v_pk_max_f16 v2, v23, v23
	v_add_u32_e32 v167, 0x8000, v167
	v_pk_max_f16 v3, v2, 0
	v_pk_max_f16 v2, v22, v22
	s_cmp_eq_u32 s10, 0
	v_pk_max_f16 v2, v2, 0
	ds_write_b128 v10, v[2:5]
	v_pk_max_f16 v3, v7, 0
	v_pk_max_f16 v2, v6, 0
	v_pk_max_f16 v4, v8, 0
	v_pk_max_f16 v5, v9, 0
	v_add_u32_e32 v6, v169, v163
	v_add_u32_e32 v163, 0x8000, v163
	v_add_u32_e32 v171, 0x3000, v171
	ds_write_b128 v6, v[2:5]
	s_setprio 0
	s_cbranch_scc1 .LBB3_82

.LBB4_80:
	s_setprio 0
	v_lshlrev_b64 v[6:7], 9, v[168:169]
	v_or_b32_e32 v6, v6, v198
	v_lshl_add_u64 v[2:3], s[20:21], 0, v[6:7]
	global_load_dwordx4 v[2:5], v[2:3], off nt
	v_lshl_add_u64 v[6:7], s[22:23], 0, v[6:7]
	global_load_dwordx4 v[6:9], v[6:7], off nt
	v_add_u32_e32 v168, v185, v199
	v_lshlrev_b64 v[26:27], 9, v[168:169]
	v_or_b32_e32 v26, v26, v198
	v_lshl_add_u64 v[22:23], s[20:21], 0, v[26:27]
	global_load_dwordx4 v[22:25], v[22:23], off nt
	v_lshl_add_u64 v[26:27], s[22:23], 0, v[26:27]
	global_load_dwordx4 v[26:29], v[26:27], off nt
	v_pk_add_f16 v17, v17, v33
	v_pk_add_f16 v16, v16, v32
	v_pk_add_f16 v15, v15, v31
	v_pk_add_f16 v14, v14, v30
	v_pk_fma_f16 v42, v13, v33, v21
	v_pk_fma_f16 v43, v12, v32, v20
	v_rcp_f16_e32 v12, v14
	v_rcp_f16_sdwa v13, v14 dst_sel:DWORD dst_unused:UNUSED_PAD src0_sel:WORD_1
	v_rcp_f16_e32 v14, v15
	v_rcp_f16_sdwa v15, v15 dst_sel:DWORD dst_unused:UNUSED_PAD src0_sel:WORD_1
	v_rcp_f16_e32 v46, v16
	v_rcp_f16_sdwa v16, v16 dst_sel:DWORD dst_unused:UNUSED_PAD src0_sel:WORD_1
	v_rcp_f16_e32 v47, v17
	v_rcp_f16_sdwa v17, v17 dst_sel:DWORD dst_unused:UNUSED_PAD src0_sel:WORD_1
	v_add_u32_e32 v168, v187, v199
	v_pk_fma_f16 v44, v10, v30, v18
	v_pk_fma_f16 v45, v11, v31, v19
	v_lshlrev_b64 v[10:11], 9, v[168:169]
	v_or_b32_e32 v10, v10, v198
	v_lshl_add_u64 v[38:39], s[20:21], 0, v[10:11]
	v_lshl_add_u64 v[40:41], s[22:23], 0, v[10:11]
	v_pack_b32_f16 v48, v14, v15
	v_pack_b32_f16 v49, v12, v13
	v_pack_b32_f16 v46, v46, v16
	v_pack_b32_f16 v47, v47, v17
	global_load_dwordx4 v[10:13], v[38:39], off nt
	global_load_dwordx4 v[14:17], v[40:41], off nt
	v_cvt_f32_f16_sdwa v21, v139 dst_sel:DWORD dst_unused:UNUSED_PAD src0_sel:WORD_1
	v_cvt_f32_f16_e32 v20, v139
	v_cvt_f32_f16_sdwa v19, v138 dst_sel:DWORD dst_unused:UNUSED_PAD src0_sel:WORD_1
	v_cvt_f32_f16_e32 v18, v138
	v_cvt_f32_f16_sdwa v33, v141 dst_sel:DWORD dst_unused:UNUSED_PAD src0_sel:WORD_1
	v_cvt_f32_f16_e32 v32, v141
	v_pk_mul_f16 v58, v43, v46
	v_pk_mul_f16 v59, v42, v47
	v_cvt_f32_f16_sdwa v31, v140 dst_sel:DWORD dst_unused:UNUSED_PAD src0_sel:WORD_1
	v_cvt_f32_f16_e32 v30, v140
	v_pk_mul_f16 v52, v45, v48
	v_pk_mul_f16 v53, v44, v49
	v_add_u32_e32 v168, v190, v199
	v_lshlrev_b64 v[36:37], 9, v[168:169]
	v_or_b32_e32 v36, v36, v198
	v_lshl_or_b32 v50, s46, 6, v178
	v_lshlrev_b32_e32 v51, 9, v50
	v_add_u32_e32 v203, v184, v51
	v_cvt_f32_f16_sdwa v35, v77 dst_sel:DWORD dst_unused:UNUSED_PAD src0_sel:WORD_1
	v_cvt_f32_f16_e32 v34, v77
	v_add_lshl_u32 v202, v188, v50, 9
	s_mov_b64 s[4:5], -1
	s_and_b64 vcc, exec, s[26:27]
	s_waitcnt vmcnt(5)
	v_cvt_f32_f16_e32 v38, v2
	v_cvt_f32_f16_sdwa v39, v2 dst_sel:DWORD dst_unused:UNUSED_PAD src0_sel:WORD_1
	v_cvt_f32_f16_e32 v2, v3
	v_cvt_f32_f16_sdwa v3, v3 dst_sel:DWORD dst_unused:UNUSED_PAD src0_sel:WORD_1
	s_waitcnt vmcnt(4)
	v_cvt_f32_f16_e32 v40, v6
	v_cvt_f32_f16_sdwa v41, v6 dst_sel:DWORD dst_unused:UNUSED_PAD src0_sel:WORD_1
	v_cvt_f32_f16_e32 v6, v7
	v_cvt_f32_f16_sdwa v7, v7 dst_sel:DWORD dst_unused:UNUSED_PAD src0_sel:WORD_1
	v_cvt_f32_f16_e32 v42, v4
	v_cvt_f32_f16_sdwa v43, v4 dst_sel:DWORD dst_unused:UNUSED_PAD src0_sel:WORD_1
	v_cvt_f32_f16_e32 v4, v5
	v_cvt_f32_f16_sdwa v5, v5 dst_sel:DWORD dst_unused:UNUSED_PAD src0_sel:WORD_1
	v_cvt_f32_f16_e32 v44, v8
	v_cvt_f32_f16_sdwa v45, v8 dst_sel:DWORD dst_unused:UNUSED_PAD src0_sel:WORD_1
	v_cvt_f32_f16_e32 v8, v9
	v_cvt_f32_f16_sdwa v9, v9 dst_sel:DWORD dst_unused:UNUSED_PAD src0_sel:WORD_1
	v_pk_add_f32 v[2:3], v[20:21], v[2:3]
	v_pk_add_f32 v[18:19], v[18:19], v[38:39]
	v_pk_add_f32 v[4:5], v[32:33], v[4:5]
	v_pk_add_f32 v[6:7], v[2:3], v[6:7]
	v_pk_add_f32 v[20:21], v[30:31], v[42:43]
	v_pk_add_f32 v[18:19], v[18:19], v[40:41]
	v_pk_add_f32 v[8:9], v[4:5], v[8:9]
	v_cvt_pk_f16_f32 v3, v6, v7
	v_lshl_add_u64 v[6:7], s[20:21], 0, v[36:37]
	v_pk_add_f32 v[20:21], v[20:21], v[44:45]
	v_cvt_pk_f16_f32 v2, v18, v19
	v_cvt_pk_f16_f32 v5, v8, v9
	global_load_dwordx4 v[6:9], v[6:7], off nt
	v_lshl_add_u64 v[18:19], s[22:23], 0, v[36:37]
	v_cvt_pk_f16_f32 v4, v20, v21
	global_load_dwordx4 v[18:21], v[18:19], off nt
	s_waitcnt vmcnt(5)
	v_cvt_f32_f16_e32 v46, v22
	v_cvt_f32_f16_sdwa v47, v22 dst_sel:DWORD dst_unused:UNUSED_PAD src0_sel:WORD_1
	ds_write_b128 v203, v[2:5]
	v_cvt_f32_f16_sdwa v5, v76 dst_sel:DWORD dst_unused:UNUSED_PAD src0_sel:WORD_1
	v_cvt_f32_f16_e32 v4, v76
	v_cvt_f32_f16_e32 v22, v23
	v_cvt_f32_f16_sdwa v23, v23 dst_sel:DWORD dst_unused:UNUSED_PAD src0_sel:WORD_1
	s_waitcnt vmcnt(4)
	v_cvt_f32_f16_e32 v48, v26
	v_cvt_f32_f16_sdwa v49, v26 dst_sel:DWORD dst_unused:UNUSED_PAD src0_sel:WORD_1
	v_cvt_f32_f16_e32 v26, v27
	v_cvt_f32_f16_sdwa v27, v27 dst_sel:DWORD dst_unused:UNUSED_PAD src0_sel:WORD_1
	v_cvt_f32_f16_sdwa v31, v75 dst_sel:DWORD dst_unused:UNUSED_PAD src0_sel:WORD_1
	v_cvt_f32_f16_e32 v30, v75
	v_cvt_f32_f16_e32 v32, v24
	v_cvt_f32_f16_sdwa v33, v24 dst_sel:DWORD dst_unused:UNUSED_PAD src0_sel:WORD_1
	v_pk_add_f32 v[4:5], v[4:5], v[22:23]
	v_cvt_f32_f16_e32 v22, v28
	v_pk_add_f32 v[4:5], v[4:5], v[26:27]
	v_cvt_f32_f16_sdwa v23, v28 dst_sel:DWORD dst_unused:UNUSED_PAD src0_sel:WORD_1
	v_cvt_f32_f16_sdwa v27, v74 dst_sel:DWORD dst_unused:UNUSED_PAD src0_sel:WORD_1
	v_cvt_f32_f16_e32 v26, v74
	v_cvt_f32_f16_e32 v24, v25
	v_cvt_f32_f16_sdwa v25, v25 dst_sel:DWORD dst_unused:UNUSED_PAD src0_sel:WORD_1
	v_pk_add_f32 v[2:3], v[34:35], v[46:47]
	v_cvt_f32_f16_e32 v28, v29
	v_cvt_f32_f16_sdwa v29, v29 dst_sel:DWORD dst_unused:UNUSED_PAD src0_sel:WORD_1
	v_pk_add_f32 v[2:3], v[2:3], v[48:49]
	s_nop 0
	v_cvt_pk_f16_f32 v2, v2, v3
	v_cvt_pk_f16_f32 v3, v4, v5
	v_pk_add_f32 v[4:5], v[30:31], v[32:33]
	s_nop 0
	v_pk_add_f32 v[4:5], v[4:5], v[22:23]
	v_pk_add_f32 v[22:23], v[26:27], v[24:25]
	v_cvt_pk_f16_f32 v4, v4, v5
	v_pk_add_f32 v[22:23], v[22:23], v[28:29]
	s_waitcnt vmcnt(3)
	v_cvt_f32_f16_e32 v24, v10
	v_cvt_pk_f16_f32 v5, v22, v23
	v_add_u32_e32 v22, v186, v50
	v_lshlrev_b32_e32 v204, 9, v22
	v_bitop3_b32 v22, v22, v179, 15 bitop3:0x6c
	v_lshlrev_b32_e32 v205, 4, v22
	v_cvt_f32_f16_sdwa v25, v10 dst_sel:DWORD dst_unused:UNUSED_PAD src0_sel:WORD_1
	v_or_b32_e32 v10, v205, v204
	v_cvt_f32_f16_sdwa v23, v57 dst_sel:DWORD dst_unused:UNUSED_PAD src0_sel:WORD_1
	v_cvt_f32_f16_e32 v22, v57
	ds_write_b128 v10, v[2:5]
	v_cvt_f32_f16_sdwa v5, v56 dst_sel:DWORD dst_unused:UNUSED_PAD src0_sel:WORD_1
	v_cvt_f32_f16_e32 v4, v56
	v_cvt_f32_f16_e32 v10, v11
	v_cvt_f32_f16_sdwa v11, v11 dst_sel:DWORD dst_unused:UNUSED_PAD src0_sel:WORD_1
	s_waitcnt vmcnt(2)
	v_cvt_f32_f16_e32 v26, v14
	v_cvt_f32_f16_sdwa v27, v14 dst_sel:DWORD dst_unused:UNUSED_PAD src0_sel:WORD_1
	v_cvt_f32_f16_e32 v14, v15
	v_cvt_f32_f16_sdwa v15, v15 dst_sel:DWORD dst_unused:UNUSED_PAD src0_sel:WORD_1
	v_pk_add_f32 v[2:3], v[22:23], v[24:25]
	v_cvt_f32_f16_sdwa v23, v55 dst_sel:DWORD dst_unused:UNUSED_PAD src0_sel:WORD_1
	v_cvt_f32_f16_e32 v22, v55
	v_cvt_f32_f16_e32 v24, v12
	v_cvt_f32_f16_sdwa v25, v12 dst_sel:DWORD dst_unused:UNUSED_PAD src0_sel:WORD_1
	v_pk_add_f32 v[4:5], v[4:5], v[10:11]
	v_cvt_f32_f16_e32 v10, v16
	v_pk_add_f32 v[4:5], v[4:5], v[14:15]
	v_cvt_f32_f16_sdwa v11, v16 dst_sel:DWORD dst_unused:UNUSED_PAD src0_sel:WORD_1
	v_cvt_f32_f16_sdwa v15, v54 dst_sel:DWORD dst_unused:UNUSED_PAD src0_sel:WORD_1
	v_cvt_f32_f16_e32 v14, v54
	v_cvt_f32_f16_e32 v12, v13
	v_cvt_f32_f16_sdwa v13, v13 dst_sel:DWORD dst_unused:UNUSED_PAD src0_sel:WORD_1
	v_cvt_f32_f16_e32 v16, v17
	v_cvt_f32_f16_sdwa v17, v17 dst_sel:DWORD dst_unused:UNUSED_PAD src0_sel:WORD_1
	v_pk_add_f32 v[2:3], v[2:3], v[26:27]
	s_nop 0
	v_cvt_pk_f16_f32 v2, v2, v3
	v_cvt_pk_f16_f32 v3, v4, v5
	v_pk_add_f32 v[4:5], v[22:23], v[24:25]
	s_nop 0
	v_pk_add_f32 v[4:5], v[4:5], v[10:11]
	v_pk_add_f32 v[10:11], v[14:15], v[12:13]
	v_cvt_pk_f16_f32 v4, v4, v5
	v_pk_add_f32 v[10:11], v[10:11], v[16:17]
	s_waitcnt vmcnt(1)
	v_cvt_f32_f16_e32 v12, v6
	v_cvt_pk_f16_f32 v5, v10, v11
	v_cvt_f32_f16_e32 v10, v53
	v_cvt_f32_f16_sdwa v11, v53 dst_sel:DWORD dst_unused:UNUSED_PAD src0_sel:WORD_1
	v_cvt_f32_f16_sdwa v13, v6 dst_sel:DWORD dst_unused:UNUSED_PAD src0_sel:WORD_1
	s_waitcnt vmcnt(0)
	v_cvt_f32_f16_e32 v14, v18
	v_cvt_f32_f16_sdwa v15, v18 dst_sel:DWORD dst_unused:UNUSED_PAD src0_sel:WORD_1
	v_or_b32_e32 v6, v189, v202
	ds_write_b128 v6, v[2:5]
	v_cvt_f32_f16_e32 v4, v52
	v_cvt_f32_f16_sdwa v5, v52 dst_sel:DWORD dst_unused:UNUSED_PAD src0_sel:WORD_1
	v_cvt_f32_f16_e32 v6, v7
	v_cvt_f32_f16_sdwa v7, v7 dst_sel:DWORD dst_unused:UNUSED_PAD src0_sel:WORD_1
	v_pk_add_f32 v[2:3], v[10:11], v[12:13]
	v_cvt_f32_f16_e32 v10, v19
	v_cvt_f32_f16_sdwa v11, v19 dst_sel:DWORD dst_unused:UNUSED_PAD src0_sel:WORD_1
	v_pk_add_f32 v[2:3], v[2:3], v[14:15]
	v_cvt_f32_f16_e32 v12, v58
	v_cvt_f32_f16_sdwa v13, v58 dst_sel:DWORD dst_unused:UNUSED_PAD src0_sel:WORD_1
	v_cvt_f32_f16_e32 v14, v8
	v_cvt_f32_f16_sdwa v15, v8 dst_sel:DWORD dst_unused:UNUSED_PAD src0_sel:WORD_1
	v_pk_add_f32 v[4:5], v[4:5], v[6:7]
	v_cvt_f32_f16_e32 v6, v20
	v_pk_add_f32 v[4:5], v[4:5], v[10:11]
	v_cvt_f32_f16_sdwa v7, v20 dst_sel:DWORD dst_unused:UNUSED_PAD src0_sel:WORD_1
	v_cvt_f32_f16_e32 v10, v59
	v_cvt_f32_f16_sdwa v11, v59 dst_sel:DWORD dst_unused:UNUSED_PAD src0_sel:WORD_1
	v_cvt_f32_f16_e32 v8, v9
	v_cvt_f32_f16_sdwa v9, v9 dst_sel:DWORD dst_unused:UNUSED_PAD src0_sel:WORD_1
	v_cvt_pk_f16_f32 v2, v2, v3
	v_cvt_pk_f16_f32 v3, v4, v5
	v_pk_add_f32 v[4:5], v[12:13], v[14:15]
	v_cvt_f32_f16_e32 v12, v21
	v_cvt_f32_f16_sdwa v13, v21 dst_sel:DWORD dst_unused:UNUSED_PAD src0_sel:WORD_1
	v_pk_add_f32 v[4:5], v[4:5], v[6:7]
	v_pk_add_f32 v[6:7], v[10:11], v[8:9]
	v_cvt_pk_f16_f32 v4, v4, v5
	v_pk_add_f32 v[6:7], v[6:7], v[12:13]
	s_nop 0
	v_cvt_pk_f16_f32 v5, v6, v7
	v_add_lshl_u32 v6, v191, v50, 9
	v_add_u32_e32 v168, v192, v6
	ds_write_b128 v168, v[2:5]
	global_load_dwordx4 v[2:5], v[174:175], off
	global_load_dwordx4 v[8:11], v[176:177], off
	global_load_dwordx4 v[12:15], v[174:175], off offset:16
	global_load_dwordx4 v[16:19], v[176:177], off offset:16
	s_cbranch_vccz .LBB4_118
	global_load_dwordx3 v[154:156], v169, s[18:19]
	s_mov_b32 s14, s38
	s_mov_b32 s15, s39
	v_cmp_lt_u32_e64 s[64:65], 0, v199
	v_cmp_gt_u32_e64 s[66:67], 63, v199
	v_cmp_lt_u32_e64 s[68:69], 0, v180
	v_cmp_gt_u32_e64 s[70:71], 60, v180
	buffer_load_dwordx4 v[210:213], v200, s[12:15], 0 offen
	s_and_b64 s[72:73], s[68:69], s[64:65]
	s_and_b64 s[74:75], s[68:69], s[66:67]
	s_and_b64 s[76:77], s[70:71], s[64:65]
	s_and_b64 s[78:79], s[70:71], s[66:67]
	v_add_u32_e32 v245, 0xfffe7c00, v200
	v_add_u32_e32 v246, 0xfffe8000, v200
	s_mov_b64 exec, s[72:73]
	buffer_load_dwordx4 v[122:125], v245, s[12:15], 0 offen
	buffer_load_dwordx4 v[82:85], v245, s[12:15], 0 offen offset:512
	s_mov_b64 exec, -1
	s_mov_b64 exec, s[68:69]
	buffer_load_dwordx4 v[138:141], v246, s[12:15], 0 offen offset:512
	buffer_load_dwordx4 v[106:109], v246, s[12:15], 0 offen offset:1024
	s_mov_b64 exec, -1
	s_mov_b64 exec, s[74:75]
	buffer_load_dwordx4 v[146:149], v246, s[12:15], 0 offen offset:2048
	buffer_load_dwordx4 v[126:129], v246, s[12:15], 0 offen offset:2560
	s_mov_b64 exec, -1
	v_add_u32_e32 v245, 0xfffffc00, v200
	s_mov_b64 exec, s[64:65]
	buffer_load_dwordx4 v[94:97], v245, s[12:15], 0 offen
	buffer_load_dwordx4 v[54:57], v245, s[12:15], 0 offen offset:512
	s_mov_b64 exec, -1
	buffer_load_dwordx4 v[118:121], v200, s[12:15], 0 offen offset:512
	buffer_load_dwordx4 v[74:77], v200, s[12:15], 0 offen offset:1024
	s_mov_b64 exec, s[66:67]
	buffer_load_dwordx4 v[134:137], v200, s[12:15], 0 offen offset:2048
	buffer_load_dwordx4 v[98:101], v200, s[12:15], 0 offen offset:2560
	s_mov_b64 exec, -1
	v_add_u32_e32 v245, 0x17c00, v200
	v_add_u32_e32 v246, 0x18000, v200
	s_mov_b64 exec, s[64:65]
	buffer_load_dwordx4 v[62:65], v245, s[12:15], 0 offen
	buffer_load_dwordx4 v[30:33], v245, s[12:15], 0 offen offset:512
	s_mov_b64 exec, -1
	buffer_load_dwordx4 v[78:81], v246, s[12:15], 0 offen offset:512
	buffer_load_dwordx4 v[42:45], v246, s[12:15], 0 offen offset:1024
	s_mov_b64 exec, s[66:67]
	buffer_load_dwordx4 v[102:105], v246, s[12:15], 0 offen offset:2048
	buffer_load_dwordx4 v[58:61], v246, s[12:15], 0 offen offset:2560
	s_mov_b64 exec, -1
	v_add_u32_e32 v245, 0x18000, v200
	buffer_load_dwordx4 v[162:165], v245, s[12:15], 0 offen
	v_add_u32_e32 v246, 0x30000, v200
	buffer_load_dwordx4 v[158:161], v246, s[12:15], 0 offen
	v_add_u32_e32 v245, 0x2fc00, v200
	v_add_u32_e32 v246, 0x30000, v200
	v_add_u32_e32 v247, 0x47c00, v200
	v_add_u32_e32 v248, 0x48000, v200
	v_add_u32_e32 v249, 0x5fc00, v200
	v_add_u32_e32 v250, 0x60000, v200
	s_waitcnt vmcnt(22)
	v_cvt_pk_f16_f32 v6, v2, v3
	v_cvt_pk_f16_f32 v2, v8, v9
	v_cvt_pk_f16_f32 v7, v4, v5
	v_cvt_pk_f16_f32 v3, v10, v11
	v_cvt_pk_f16_f32 v8, v12, v13
	v_cvt_pk_f16_f32 v4, v16, v17
	v_cvt_pk_f16_f32 v9, v14, v15
	v_cvt_pk_f16_f32 v5, v18, v19
	s_not_b64 exec, s[72:73]
	s_cbranch_execz .Lmyf_C3_0
	v_mov_b32_e32 v122, v6
	v_mov_b32_e32 v123, v7
	v_mov_b32_e32 v124, v8
	v_mov_b32_e32 v125, v9
	v_mov_b32_e32 v82, v2
	v_mov_b32_e32 v83, v3
	v_mov_b32_e32 v84, v4
	v_mov_b32_e32 v85, v5
